# speedup vs baseline: 1.0051x; 1.0026x over previous
_ZN2pw16attn_fwd_pwg4x64EPKtS1_S1_Pf:
	s_cmp_lg_u32 0, -1
	v_lshrrev_b32_e32 v1, 6, v0
	s_cselect_b32 s3, 0, 0
	v_lshl_add_u32 v2, v1, 12, s3
	s_mov_b32 s25, 0
	v_readfirstlane_b32 s30, v2
	s_cmpk_gt_u32 s2, 0xff
	v_readfirstlane_b32 s3, v1
	s_cbranch_scc1 .LBB2_64
	v_bfe_u32 v2, v0, 5, 1
	v_lshlrev_b32_e32 v3, 8, v0
	v_and_b32_e32 v4, 7, v0
	v_and_b32_e32 v3, 0x1f00, v3
	v_bitop3_b32 v5, v2, v0, 7 bitop3:0x78
	v_bitop3_b32 v6, v2, v4, 2 bitop3:0x36
	v_bitop3_b32 v7, v2, v4, 4 bitop3:0x36
	v_bitop3_b32 v4, v2, v4, 6 bitop3:0x36
	v_lshl_or_b32 v5, v5, 4, v3
	v_lshl_or_b32 v6, v6, 4, v3
	v_lshl_or_b32 v7, v7, 4, v3
	v_lshl_or_b32 v3, v4, 4, v3
	v_and_b32_e32 v4, 3, v0
	v_lshlrev_b32_e32 v9, 4, v0
	v_lshlrev_b32_e32 v8, 3, v4
	v_and_b32_e32 v9, 0xc0, v9
	v_lshlrev_b32_e32 v11, 1, v0
	v_lshlrev_b32_e32 v12, 8, v2
	v_and_b32_e32 v11, 32, v11
	v_or3_b32 v8, v8, v12, v9
	s_mov_b32 s5, 0x8000
	v_bfe_u32 v10, v0, 4, 2
	v_or3_b32 v8, v8, v11, s5
	v_and_b32_e32 v11, 15, v0
	s_load_dwordx8 s[8:15], s[0:1], 0x0
	v_lshlrev_b32_e32 v9, 11, v10
	v_bitop3_b32 v12, v10, v0, 15 bitop3:0x78
	v_bitop3_b32 v10, v10, v11, 4 bitop3:0x36
	s_load_dword s34, s[0:1], 0x20
	s_cmp_lg_u32 0, -1
	v_lshl_or_b32 v209, v12, 4, v9
	v_lshl_or_b32 v210, v10, 4, v9
	v_lshlrev_b32_e32 v9, 9, v0
	s_cselect_b32 s4, 0, 0
	v_and_b32_e32 v9, 0x3800, v9
	v_lshlrev_b32_e32 v2, 6, v2
	v_lshlrev_b32_e32 v4, 4, v4
	v_lshlrev_b32_e32 v212, 14, v1
	s_add_i32 s0, 0, 0x20000
	v_add_u32_e32 v204, s4, v5
	v_add_u32_e32 v205, s4, v6
	v_add_u32_e32 v206, s4, v7
	v_add_u32_e32 v207, s4, v3
	v_add_u32_e32 v208, s4, v8
	v_or3_b32 v211, v9, v2, v4
	s_lshl_b32 s33, s3, 15
	s_mov_b32 s3, s25
	v_or_b32_e32 v2, 0x10000, v212
	v_lshl_add_u32 v214, v1, 13, s0
	s_lshl_b32 s0, s2, 8
	s_addk_i32 s4, 0x4000
	s_add_i32 s31, s30, 0x8000
	v_and_b32_e32 v213, 0xc0, v0
	s_mov_b32 s7, 0x20000
	s_and_b32 s35, s0, 0x700
	v_add_u32_e32 v215, v2, v204
	v_add_u32_e32 v216, v2, v205
	v_add_u32_e32 v217, v2, v206
	v_add_u32_e32 v218, v2, v207
	s_add_i32 s36, s33, 0x40000
	s_add_i32 s37, s30, 0x400
	s_add_i32 s38, s33, 0x42000
	s_add_i32 s39, s30, 0x800
	s_add_i32 s40, s33, 0x44000
	s_add_i32 s41, s30, 0xc00
	s_add_i32 s42, s33, 0x46000
	s_add_i32 s43, s30, 0xc000
	s_add_i32 s44, s33, 0x20000
	s_add_i32 s45, s30, 0xc400
	s_add_i32 s46, s33, 0x20080
	s_add_i32 s47, s30, 0xc800
	s_add_i32 s48, s33, 0x24000
	s_add_i32 s49, s30, 0xcc00
	s_add_i32 s50, s33, 0x24080
	v_add_u32_e32 v219, s4, v5
	v_add_u32_e32 v220, s4, v6
	v_add_u32_e32 v221, s4, v7
	v_add_u32_e32 v222, s4, v3
	s_add_i32 s51, s30, 0x4000
	s_add_i32 s52, s33, 0x60000
	s_add_i32 s53, s30, 0x4400
	s_add_i32 s54, s33, 0x62000
	s_add_i32 s55, s30, 0x4800
	s_add_i32 s56, s33, 0x64000
	s_add_i32 s57, s30, 0x4c00
	s_add_i32 s58, s33, 0x66000
	s_add_i32 s59, s30, 0x8400
	s_add_i32 s60, s33, 0x40080
	s_add_i32 s61, s30, 0x8800
	s_add_i32 s62, s30, 0x8c00
	s_add_i32 s63, s33, 0x44080
	v_add_u32_e32 v223, s4, v8
	s_mov_b32 s18, 0x400000
	s_add_i32 s64, s33, 0x400000
	s_add_i32 s65, s33, 0x402000
	s_add_i32 s66, s33, 0x404000
	s_add_i32 s67, s33, 0x406000
	s_add_i32 s68, s33, 0x3e0000
	s_add_i32 s69, s33, 0x3e0080
	s_add_i32 s70, s33, 0x3e4000
	s_add_i32 s71, s33, 0x3e4080
	s_add_i32 s72, s33, 0x420000
	s_add_i32 s73, s33, 0x422000
	s_add_i32 s74, s33, 0x424000
	s_add_i32 s75, s33, 0x426000
	s_add_i32 s76, s33, 0x400080
	s_add_i32 s77, s33, 0x404080
	s_add_i32 s78, s33, 0xa6000
	v_mov_b32_e32 v201, 0
	v_mov_b32_e32 v224, 0x3e0293ee
	s_mov_b32 s79, 0x41000000
	s_movk_i32 s80, 0xf0
	v_mov_b64_e32 v[202:203], 0xff
	s_mov_b64 s[26:27], s[2:3]
	s_branch .LBB2_3
.LBB2_3:
	s_lshr_b64 s[16:17], s[26:27], 6
	s_lshl_b64 s[28:29], s[16:17], 14
	s_and_b32 s24, s26, 7
	s_or_b64 s[0:1], s[28:29], s[24:25]
	s_lshl_b64 s[0:1], s[0:1], 8
	s_waitcnt lgkmcnt(0)
	s_add_u32 s4, s10, s0
	s_addc_u32 s5, s11, s1
	s_add_u32 s20, s12, s0
	s_addc_u32 s19, s13, s1
	s_cmp_eq_u64 s[26:27], s[2:3]
	s_cselect_b64 s[0:1], -1, 0
	s_cmp_lg_u64 s[26:27], s[2:3]
	v_readfirstlane_b32 s81, v212
	s_mov_b64 s[22:23], -1
	v_mbcnt_lo_u32_b32 v225, -1, 0
	v_mbcnt_hi_u32_b32 v225, -1, v225
	s_cbranch_scc0 .LBB2_5
	s_waitcnt vmcnt(32)
	s_mov_b64 s[22:23], 0

.LBB2_26:
	s_waitcnt lgkmcnt(0)
	ds_read_b64_tr_b16 v[156:157], v223 offset:0
	ds_read_b64_tr_b16 v[158:159], v223 offset:0x800
	ds_read_b64_tr_b16 v[152:153], v223 offset:0x200
	ds_read_b64_tr_b16 v[154:155], v223 offset:0xa00
	ds_read_b64_tr_b16 v[148:149], v223 offset:0x400
	ds_read_b64_tr_b16 v[150:151], v223 offset:0xc00
	ds_read_b64_tr_b16 v[144:145], v223 offset:0x600
	ds_read_b64_tr_b16 v[146:147], v223 offset:0xe00
	ds_read_b64_tr_b16 v[140:141], v223 offset:0x1000
	ds_read_b64_tr_b16 v[142:143], v223 offset:0x1800
	ds_read_b64_tr_b16 v[136:137], v223 offset:0x1200
	ds_read_b64_tr_b16 v[138:139], v223 offset:0x1a00
	ds_read_b64_tr_b16 v[132:133], v223 offset:0x1400
	ds_read_b64_tr_b16 v[134:135], v223 offset:0x1c00
	ds_read_b64_tr_b16 v[128:129], v223 offset:0x1600
	ds_read_b64_tr_b16 v[130:131], v223 offset:0x1e00
	ds_read_b64_tr_b16 v[124:125], v223 offset:0x2000
	ds_read_b64_tr_b16 v[126:127], v223 offset:0x2800
	v_exp_f32_e32 v48, v48
	v_exp_f32_e32 v49, v49
	ds_read_b64_tr_b16 v[120:121], v223 offset:0x2200
	ds_read_b64_tr_b16 v[122:123], v223 offset:0x2a00
	ds_read_b64_tr_b16 v[116:117], v223 offset:0x2400
	ds_read_b64_tr_b16 v[118:119], v223 offset:0x2c00
	v_exp_f32_e32 v190, v44
	v_cvt_pk_bf16_f32 v44, v48, v49
	v_add_f32_e32 v48, v161, v48
	v_add_f32_e32 v49, v160, v49
	ds_read_b64_tr_b16 v[112:113], v223 offset:0x2600
	v_exp_f32_e32 v164, v50
	v_exp_f32_e32 v165, v51
	v_add_f32_e32 v48, v48, v164
	v_add_f32_e32 v49, v49, v165
	ds_read_b64_tr_b16 v[114:115], v223 offset:0x2e00
	v_exp_f32_e32 v166, v52
	v_exp_f32_e32 v167, v53
	v_add_f32_e32 v48, v48, v166
	v_add_f32_e32 v49, v49, v167
	ds_read_b64_tr_b16 v[108:109], v223 offset:0x3000
	v_exp_f32_e32 v168, v54
	v_exp_f32_e32 v169, v55
	v_exp_f32_e32 v178, v32
	v_cvt_pk_bf16_f32 v51, v66, v67
	v_add_f32_e32 v48, v48, v168
	v_add_f32_e32 v49, v49, v169
	v_add_f32_e32 v66, v162, v178
	ds_read_b64_tr_b16 v[110:111], v223 offset:0x3800
	v_exp_f32_e32 v170, v56
	v_exp_f32_e32 v171, v57
	v_exp_f32_e32 v179, v33
	v_exp_f32_e32 v180, v34
	v_add_f32_e32 v48, v48, v170
	v_add_f32_e32 v49, v49, v171
	v_add_f32_e32 v67, v163, v179
	v_add_f32_e32 v66, v66, v180
	ds_read_b64_tr_b16 v[104:105], v223 offset:0x3200
	v_exp_f32_e32 v172, v58
	v_exp_f32_e32 v173, v59
	v_exp_f32_e32 v181, v35
	v_exp_f32_e32 v182, v36
	v_add_f32_e32 v48, v48, v172
	v_add_f32_e32 v49, v49, v173
	v_add_f32_e32 v67, v67, v181
	v_add_f32_e32 v66, v66, v182
	ds_read_b64_tr_b16 v[106:107], v223 offset:0x3a00
	v_exp_f32_e32 v174, v60
	v_exp_f32_e32 v175, v61
	v_exp_f32_e32 v183, v37
	v_exp_f32_e32 v184, v38
	v_add_f32_e32 v48, v48, v174
	v_add_f32_e32 v49, v49, v175
	v_add_f32_e32 v67, v67, v183
	v_add_f32_e32 v66, v66, v184
	ds_read_b64_tr_b16 v[100:101], v223 offset:0x3400
	v_exp_f32_e32 v176, v62
	v_exp_f32_e32 v177, v63
	v_exp_f32_e32 v185, v39
	v_exp_f32_e32 v186, v40
	v_add_f32_e32 v48, v48, v176
	v_add_f32_e32 v49, v49, v177
	v_add_f32_e32 v67, v67, v185
	v_add_f32_e32 v66, v66, v186
	ds_read_b64_tr_b16 v[102:103], v223 offset:0x3c00
	v_exp_f32_e32 v187, v41
	v_exp_f32_e32 v188, v42
	v_add_f32_e32 v67, v67, v187
	v_add_f32_e32 v66, v66, v188
	v_add_f32_e32 v48, v48, v49
	ds_read_b64_tr_b16 v[96:97], v223 offset:0x3600
	v_exp_f32_e32 v189, v43
	v_mov_b32_e32 v49, v48
	v_exp_f32_e32 v191, v45
	v_exp_f32_e32 v192, v46
	v_exp_f32_e32 v193, v47
	v_add_f32_e32 v67, v67, v189
	v_add_f32_e32 v66, v66, v190
	v_permlane32_swap_b32_e32 v48, v49
	ds_read_b64_tr_b16 v[98:99], v223 offset:0x3e00
	s_nop 1
	s_nop 1
	s_nop 1
	s_nop 1
	s_nop 1
	s_nop 1
	s_nop 1
	s_nop 1
	s_nop 1
	s_nop 1
	s_nop 1
	s_nop 1
	s_nop 1
	s_nop 1
	v_add_f32_e32 v67, v67, v191
	s_nop 1
	v_add_f32_e32 v66, v66, v192
	s_nop 1
	v_add_f32_e32 v48, v48, v49
	s_waitcnt lgkmcnt(0)
	s_nop 0
	v_cvt_pk_bf16_f32 v50, v64, v65
	v_add_f32_e32 v67, v67, v193
	v_add_f32_e32 v49, v231, v48
	v_cvt_pk_bf16_f32 v52, v68, v69
	v_add_f32_e32 v48, v66, v67
	v_cvt_pk_bf16_f32 v36, v72, v73
	v_mov_b32_e32 v66, v48
	s_nop 1
	v_permlane32_swap_b32_e32 v48, v66
	v_cvt_pk_bf16_f32 v37, v74, v75
	v_cvt_pk_bf16_f32 v38, v76, v77
	v_cvt_pk_bf16_f32 v39, v78, v79
	v_cvt_pk_bf16_f32 v45, v164, v165
	v_cvt_pk_bf16_f32 v46, v166, v167
	v_cvt_pk_bf16_f32 v47, v168, v169
	v_cvt_pk_bf16_f32 v32, v170, v171
	v_cvt_pk_bf16_f32 v33, v172, v173
	v_cvt_pk_bf16_f32 v34, v174, v175
	v_cvt_pk_bf16_f32 v35, v176, v177
	v_cvt_pk_bf16_f32 v40, v186, v187
	v_cvt_pk_bf16_f32 v41, v188, v189
	v_cvt_pk_bf16_f32 v42, v190, v191
	v_cvt_pk_bf16_f32 v43, v192, v193
	v_add_f32_e32 v48, v48, v66
	v_cvt_pk_bf16_f32 v53, v70, v71
	v_cvt_pk_bf16_f32 v54, v80, v81
	v_cvt_pk_bf16_f32 v55, v82, v83
	v_cvt_pk_bf16_f32 v56, v84, v85
	v_cvt_pk_bf16_f32 v57, v86, v87
	v_cvt_pk_bf16_f32 v58, v88, v89
	v_cvt_pk_bf16_f32 v59, v90, v91
	v_cvt_pk_bf16_f32 v60, v92, v93
	v_cvt_pk_bf16_f32 v61, v94, v95
	v_cvt_pk_bf16_f32 v62, v178, v179
	v_cvt_pk_bf16_f32 v63, v180, v181
	v_cvt_pk_bf16_f32 v64, v182, v183
	v_cvt_pk_bf16_f32 v65, v184, v185
	v_add_f32_e32 v48, v230, v48
	s_nop 1
	v_mfma_f32_32x32x16_bf16 a[0:15], v[156:159], v[50:53], a[0:15]
	s_nop 0
	v_mfma_f32_32x32x16_bf16 a[16:31], v[156:159], v[54:57], a[16:31]
	s_nop 0
	v_mfma_f32_32x32x16_bf16 a[32:47], v[152:155], v[50:53], a[32:47]
	s_nop 0
	v_mfma_f32_32x32x16_bf16 a[48:63], v[152:155], v[54:57], a[48:63]
	s_nop 0
	v_mfma_f32_32x32x16_bf16 a[64:79], v[148:151], v[50:53], a[64:79]
	s_nop 0
	v_mfma_f32_32x32x16_bf16 a[80:95], v[148:151], v[54:57], a[80:95]
	s_nop 0
	v_mfma_f32_32x32x16_bf16 a[96:111], v[144:147], v[50:53], a[96:111]
	s_nop 0
	v_mfma_f32_32x32x16_bf16 a[112:127], v[144:147], v[54:57], a[112:127]
	s_nop 0
	v_mfma_f32_32x32x16_bf16 a[0:15], v[140:143], v[36:39], a[0:15]
	s_nop 0
	v_mfma_f32_32x32x16_bf16 a[16:31], v[140:143], v[58:61], a[16:31]
	s_nop 0
	v_mfma_f32_32x32x16_bf16 a[32:47], v[136:139], v[36:39], a[32:47]
	s_nop 0
	v_mfma_f32_32x32x16_bf16 a[48:63], v[136:139], v[58:61], a[48:63]
	s_nop 0
	v_mfma_f32_32x32x16_bf16 a[64:79], v[132:135], v[36:39], a[64:79]
	s_nop 0
	v_mfma_f32_32x32x16_bf16 a[80:95], v[132:135], v[58:61], a[80:95]
	s_nop 0
	v_mfma_f32_32x32x16_bf16 a[96:111], v[128:131], v[36:39], a[96:111]
	s_nop 0
	v_mfma_f32_32x32x16_bf16 a[112:127], v[128:131], v[58:61], a[112:127]
	s_nop 0
	v_mfma_f32_32x32x16_bf16 a[0:15], v[124:127], v[44:47], a[0:15]
	s_nop 0
	v_mfma_f32_32x32x16_bf16 a[16:31], v[124:127], v[62:65], a[16:31]
	s_nop 0
	v_mfma_f32_32x32x16_bf16 a[32:47], v[120:123], v[44:47], a[32:47]
	s_nop 0
	v_mfma_f32_32x32x16_bf16 a[48:63], v[120:123], v[62:65], a[48:63]
	s_nop 0
	v_mfma_f32_32x32x16_bf16 a[64:79], v[116:119], v[44:47], a[64:79]
	s_nop 0
	v_mfma_f32_32x32x16_bf16 a[80:95], v[116:119], v[62:65], a[80:95]
	s_nop 0
	v_mfma_f32_32x32x16_bf16 a[96:111], v[112:115], v[44:47], a[96:111]
	s_nop 0
	v_mfma_f32_32x32x16_bf16 a[112:127], v[112:115], v[62:65], a[112:127]
	s_nop 0
	v_mfma_f32_32x32x16_bf16 a[0:15], v[108:111], v[32:35], a[0:15]
	s_nop 0
	v_mfma_f32_32x32x16_bf16 a[16:31], v[108:111], v[40:43], a[16:31]
	s_nop 0
	v_mfma_f32_32x32x16_bf16 a[32:47], v[104:107], v[32:35], a[32:47]
	s_nop 0
	v_mfma_f32_32x32x16_bf16 a[48:63], v[104:107], v[40:43], a[48:63]
	s_nop 0
	v_mfma_f32_32x32x16_bf16 a[64:79], v[100:103], v[32:35], a[64:79]
	s_nop 0
	v_mfma_f32_32x32x16_bf16 a[80:95], v[100:103], v[40:43], a[80:95]
	s_nop 0
	v_mfma_f32_32x32x16_bf16 a[96:111], v[96:99], v[32:35], a[96:111]
	s_nop 0
	v_mfma_f32_32x32x16_bf16 a[112:127], v[96:99], v[40:43], a[112:127]
	v_rcp_f32_e32 v34, v49
	s_nop 7
	s_nop 7
	v_mov_b32_e32 v132, v48
	v_cmp_lt_f32_e32 vcc, 0, v49
	v_cndmask_b32_e32 v43, 0, v34, vcc
	v_lshrrev_b32_e32 v42, 4, v225
	s_lshl_b32 s4, s26, 11
	v_mov_b32_e32 v33, s29
	v_or_b32_e32 v32, s28, v200
	s_and_b32 s24, s4, 0x3800
	v_lshl_add_u64 v[34:35], s[24:25], 0, v[32:33]
	v_lshlrev_b32_e32 v39, 8, v42
	v_lshlrev_b32_e32 v32, 4, v225
	v_and_or_b32 v200, v32, s80, v39
	v_lshl_add_u64 v[32:33], s[14:15], 0, v[200:201]
	v_lshlrev_b64 v[34:35], 8, v[34:35]
	v_lshl_add_u64 v[124:125], v[32:33], 0, v[34:35]
	v_mov_b32_e32 v34, 0x1000
	v_mov_b32_e32 v35, 0
	v_lshl_add_u64 v[126:127], v[124:125], 0, v[34:35]
	v_lshl_add_u64 v[128:129], v[126:127], 0, v[34:35]
	v_lshl_add_u64 v[130:131], v[128:129], 0, v[34:35]
	v_and_b32_e32 v32, 31, v225
	v_lshl_add_u32 v36, v32, 8, v214
	v_and_b32_e32 v37, 15, v225
	v_lshlrev_b32_e32 v37, 4, v37
	v_lshrrev_b32_e32 v38, 5, v225
	v_lshlrev_b32_e32 v38, 3, v38
	v_xad_u32 v100, v38, v37, v36
	v_add_u32_e32 v101, 0x10, v38
	v_xad_u32 v101, v101, v37, v36
	v_add_u32_e32 v102, 0x20, v38
	v_xad_u32 v102, v102, v37, v36
	v_add_u32_e32 v103, 0x30, v38
	v_xad_u32 v103, v103, v37, v36
	v_add_u32_e32 v104, 0x40, v38
	v_xad_u32 v104, v104, v37, v36
	v_add_u32_e32 v105, 0x50, v38
	v_xad_u32 v105, v105, v37, v36
	v_add_u32_e32 v106, 0x60, v38
	v_xad_u32 v106, v106, v37, v36
	v_add_u32_e32 v107, 0x70, v38
	v_xad_u32 v107, v107, v37, v36
	v_add_u32_e32 v108, 0x80, v38
	v_xad_u32 v108, v108, v37, v36
	v_add_u32_e32 v109, 0x90, v38
	v_xad_u32 v109, v109, v37, v36
	v_add_u32_e32 v110, 0xa0, v38
	v_xad_u32 v110, v110, v37, v36
	v_add_u32_e32 v111, 0xb0, v38
	v_xad_u32 v111, v111, v37, v36
	v_add_u32_e32 v112, 0xc0, v38
	v_xad_u32 v112, v112, v37, v36
	v_add_u32_e32 v113, 0xd0, v38
	v_xad_u32 v113, v113, v37, v36
	v_add_u32_e32 v114, 0xe0, v38
	v_xad_u32 v114, v114, v37, v36
	v_add_u32_e32 v115, 0xf0, v38
	v_xad_u32 v115, v115, v37, v36
	v_and_b32_e32 v33, 15, v225
	v_mov_b32_e32 v116, v42
	v_and_b32_e32 v39, 15, v116
	v_xor_b32_e32 v39, v39, v33
	v_lshlrev_b32_e32 v39, 4, v39
	v_lshl_add_u32 v116, v116, 8, v214
	v_add_u32_e32 v116, v116, v39
	v_add_u32_e32 v117, 4, v42
	v_and_b32_e32 v39, 15, v117
	v_xor_b32_e32 v39, v39, v33
	v_lshlrev_b32_e32 v39, 4, v39
	v_lshl_add_u32 v117, v117, 8, v214
	v_add_u32_e32 v117, v117, v39
	v_add_u32_e32 v118, 8, v42
	v_and_b32_e32 v39, 15, v118
	v_xor_b32_e32 v39, v39, v33
	v_lshlrev_b32_e32 v39, 4, v39
	v_lshl_add_u32 v118, v118, 8, v214
	v_add_u32_e32 v118, v118, v39
	v_add_u32_e32 v119, 12, v42
	v_and_b32_e32 v39, 15, v119
	v_xor_b32_e32 v39, v39, v33
	v_lshlrev_b32_e32 v39, 4, v39
	v_lshl_add_u32 v119, v119, 8, v214
	v_add_u32_e32 v119, v119, v39
	v_add_u32_e32 v120, 16, v42
	v_and_b32_e32 v39, 15, v120
	v_xor_b32_e32 v39, v39, v33
	v_lshlrev_b32_e32 v39, 4, v39
	v_lshl_add_u32 v120, v120, 8, v214
	v_add_u32_e32 v120, v120, v39
	v_add_u32_e32 v121, 20, v42
	v_and_b32_e32 v39, 15, v121
	v_xor_b32_e32 v39, v39, v33
	v_lshlrev_b32_e32 v39, 4, v39
	v_lshl_add_u32 v121, v121, 8, v214
	v_add_u32_e32 v121, v121, v39
	v_add_u32_e32 v122, 24, v42
	v_and_b32_e32 v39, 15, v122
	v_xor_b32_e32 v39, v39, v33
	v_lshlrev_b32_e32 v39, 4, v39
	v_lshl_add_u32 v122, v122, 8, v214
	v_add_u32_e32 v122, v122, v39
	v_add_u32_e32 v123, 28, v42
	v_and_b32_e32 v39, 15, v123
	v_xor_b32_e32 v39, v39, v33
	v_lshlrev_b32_e32 v39, 4, v39
	v_lshl_add_u32 v123, v123, 8, v214
	v_add_u32_e32 v123, v123, v39
	v_accvgpr_read_b32 v64, a0
	v_accvgpr_read_b32 v65, a1
	v_accvgpr_read_b32 v66, a2
	v_accvgpr_read_b32 v67, a3
	v_accvgpr_read_b32 v68, a4
	v_accvgpr_read_b32 v69, a5
	v_accvgpr_read_b32 v70, a6
	v_accvgpr_read_b32 v71, a7
	v_accvgpr_read_b32 v72, a8
	v_accvgpr_read_b32 v73, a9
	v_accvgpr_read_b32 v74, a10
	v_accvgpr_read_b32 v75, a11
	v_accvgpr_read_b32 v76, a12
	v_accvgpr_read_b32 v77, a13
	v_accvgpr_read_b32 v78, a14
	v_accvgpr_read_b32 v79, a15
	v_mul_f32_e32 v64, v64, v43
	v_mul_f32_e32 v65, v65, v43
	v_mul_f32_e32 v66, v66, v43
	v_mul_f32_e32 v67, v67, v43
	v_mul_f32_e32 v68, v68, v43
	v_mul_f32_e32 v69, v69, v43
	v_mul_f32_e32 v70, v70, v43
	v_mul_f32_e32 v71, v71, v43
	v_mul_f32_e32 v72, v72, v43
	v_mul_f32_e32 v73, v73, v43
	v_mul_f32_e32 v74, v74, v43
	v_mul_f32_e32 v75, v75, v43
	v_mul_f32_e32 v76, v76, v43
	v_mul_f32_e32 v77, v77, v43
	v_mul_f32_e32 v78, v78, v43
	v_mul_f32_e32 v79, v79, v43
	v_cvt_pk_f16_f32 v80, v64, v65
	v_cvt_pk_f16_f32 v81, v66, v67
	v_cvt_pk_f16_f32 v82, v68, v69
	v_cvt_pk_f16_f32 v83, v70, v71
	v_cvt_pk_f16_f32 v84, v72, v73
	v_cvt_pk_f16_f32 v85, v74, v75
	v_cvt_pk_f16_f32 v86, v76, v77
	v_cvt_pk_f16_f32 v87, v78, v79
	ds_write_b64 v100, v[80:81]
	ds_write_b64 v101, v[82:83]
	ds_write_b64 v102, v[84:85]
	ds_write_b64 v103, v[86:87]
	v_accvgpr_read_b32 v64, a32
	v_accvgpr_read_b32 v65, a33
	v_accvgpr_read_b32 v66, a34
	v_accvgpr_read_b32 v67, a35
	v_accvgpr_read_b32 v68, a36
	v_accvgpr_read_b32 v69, a37
	v_accvgpr_read_b32 v70, a38
	v_accvgpr_read_b32 v71, a39
	v_accvgpr_read_b32 v72, a40
	v_accvgpr_read_b32 v73, a41
	v_accvgpr_read_b32 v74, a42
	v_accvgpr_read_b32 v75, a43
	v_accvgpr_read_b32 v76, a44
	v_accvgpr_read_b32 v77, a45
	v_accvgpr_read_b32 v78, a46
	v_accvgpr_read_b32 v79, a47
	v_mul_f32_e32 v64, v64, v43
	v_mul_f32_e32 v65, v65, v43
	v_mul_f32_e32 v66, v66, v43
	v_mul_f32_e32 v67, v67, v43
	v_mul_f32_e32 v68, v68, v43
	v_mul_f32_e32 v69, v69, v43
	v_mul_f32_e32 v70, v70, v43
	v_mul_f32_e32 v71, v71, v43
	v_mul_f32_e32 v72, v72, v43
	v_mul_f32_e32 v73, v73, v43
	v_mul_f32_e32 v74, v74, v43
	v_mul_f32_e32 v75, v75, v43
	v_mul_f32_e32 v76, v76, v43
	v_mul_f32_e32 v77, v77, v43
	v_mul_f32_e32 v78, v78, v43
	v_mul_f32_e32 v79, v79, v43
	v_cvt_pk_f16_f32 v80, v64, v65
	v_cvt_pk_f16_f32 v81, v66, v67
	v_cvt_pk_f16_f32 v82, v68, v69
	v_cvt_pk_f16_f32 v83, v70, v71
	v_cvt_pk_f16_f32 v84, v72, v73
	v_cvt_pk_f16_f32 v85, v74, v75
	v_cvt_pk_f16_f32 v86, v76, v77
	v_cvt_pk_f16_f32 v87, v78, v79
	ds_write_b64 v104, v[80:81]
	ds_write_b64 v105, v[82:83]
	ds_write_b64 v106, v[84:85]
	ds_write_b64 v107, v[86:87]
	v_accvgpr_read_b32 v64, a64
	v_accvgpr_read_b32 v65, a65
	v_accvgpr_read_b32 v66, a66
	v_accvgpr_read_b32 v67, a67
	v_accvgpr_read_b32 v68, a68
	v_accvgpr_read_b32 v69, a69
	v_accvgpr_read_b32 v70, a70
	v_accvgpr_read_b32 v71, a71
	v_accvgpr_read_b32 v72, a72
	v_accvgpr_read_b32 v73, a73
	v_accvgpr_read_b32 v74, a74
	v_accvgpr_read_b32 v75, a75
	v_accvgpr_read_b32 v76, a76
	v_accvgpr_read_b32 v77, a77
	v_accvgpr_read_b32 v78, a78
	v_accvgpr_read_b32 v79, a79
	v_mul_f32_e32 v64, v64, v43
	v_mul_f32_e32 v65, v65, v43
	v_mul_f32_e32 v66, v66, v43
	v_mul_f32_e32 v67, v67, v43
	v_mul_f32_e32 v68, v68, v43
	v_mul_f32_e32 v69, v69, v43
	v_mul_f32_e32 v70, v70, v43
	v_mul_f32_e32 v71, v71, v43
	v_mul_f32_e32 v72, v72, v43
	v_mul_f32_e32 v73, v73, v43
	v_mul_f32_e32 v74, v74, v43
	v_mul_f32_e32 v75, v75, v43
	v_mul_f32_e32 v76, v76, v43
	v_mul_f32_e32 v77, v77, v43
	v_mul_f32_e32 v78, v78, v43
	v_mul_f32_e32 v79, v79, v43
	v_cvt_pk_f16_f32 v80, v64, v65
	v_cvt_pk_f16_f32 v81, v66, v67
	v_cvt_pk_f16_f32 v82, v68, v69
	v_cvt_pk_f16_f32 v83, v70, v71
	v_cvt_pk_f16_f32 v84, v72, v73
	v_cvt_pk_f16_f32 v85, v74, v75
	v_cvt_pk_f16_f32 v86, v76, v77
	v_cvt_pk_f16_f32 v87, v78, v79
	ds_write_b64 v108, v[80:81]
	ds_write_b64 v109, v[82:83]
	ds_write_b64 v110, v[84:85]
	ds_write_b64 v111, v[86:87]
	v_accvgpr_read_b32 v64, a96
	v_accvgpr_read_b32 v65, a97
	v_accvgpr_read_b32 v66, a98
	v_accvgpr_read_b32 v67, a99
	v_accvgpr_read_b32 v68, a100
	v_accvgpr_read_b32 v69, a101
	v_accvgpr_read_b32 v70, a102
	v_accvgpr_read_b32 v71, a103
	v_accvgpr_read_b32 v72, a104
	v_accvgpr_read_b32 v73, a105
	v_accvgpr_read_b32 v74, a106
	v_accvgpr_read_b32 v75, a107
	v_accvgpr_read_b32 v76, a108
	v_accvgpr_read_b32 v77, a109
	v_accvgpr_read_b32 v78, a110
	v_accvgpr_read_b32 v79, a111
	v_mul_f32_e32 v64, v64, v43
	v_mul_f32_e32 v65, v65, v43
	v_mul_f32_e32 v66, v66, v43
	v_mul_f32_e32 v67, v67, v43
	v_mul_f32_e32 v68, v68, v43
	v_mul_f32_e32 v69, v69, v43
	v_mul_f32_e32 v70, v70, v43
	v_mul_f32_e32 v71, v71, v43
	v_mul_f32_e32 v72, v72, v43
	v_mul_f32_e32 v73, v73, v43
	v_mul_f32_e32 v74, v74, v43
	v_mul_f32_e32 v75, v75, v43
	v_mul_f32_e32 v76, v76, v43
	v_mul_f32_e32 v77, v77, v43
	v_mul_f32_e32 v78, v78, v43
	v_mul_f32_e32 v79, v79, v43
	v_cvt_pk_f16_f32 v80, v64, v65
	v_cvt_pk_f16_f32 v81, v66, v67
	v_cvt_pk_f16_f32 v82, v68, v69
	v_cvt_pk_f16_f32 v83, v70, v71
	v_cvt_pk_f16_f32 v84, v72, v73
	v_cvt_pk_f16_f32 v85, v74, v75
	v_cvt_pk_f16_f32 v86, v76, v77
	v_cvt_pk_f16_f32 v87, v78, v79
	ds_write_b64 v112, v[80:81]
	ds_write_b64 v113, v[82:83]
	ds_write_b64 v114, v[84:85]
	ds_write_b64 v115, v[86:87]
	s_waitcnt lgkmcnt(0)
	ds_read_b128 v[136:139], v116
	ds_read_b128 v[140:143], v117
	ds_read_b128 v[144:147], v118
	ds_read_b128 v[148:151], v119
	ds_read_b128 v[152:155], v120
	ds_read_b128 v[156:159], v121
	ds_read_b128 v[160:163], v122
	ds_read_b128 v[164:167], v123
	s_waitcnt lgkmcnt(7)
	global_store_dwordx4 v[124:125], v[136:139], off sc1
	s_waitcnt lgkmcnt(6)
	global_store_dwordx4 v[124:125], v[140:143], off offset:1024 sc1
	s_waitcnt lgkmcnt(5)
	global_store_dwordx4 v[124:125], v[144:147], off offset:2048 sc1
	s_waitcnt lgkmcnt(4)
	global_store_dwordx4 v[124:125], v[148:151], off offset:3072 sc1
	s_waitcnt lgkmcnt(3)
	global_store_dwordx4 v[126:127], v[152:155], off sc1
	s_waitcnt lgkmcnt(2)
	global_store_dwordx4 v[126:127], v[156:159], off offset:1024 sc1
	s_waitcnt lgkmcnt(1)
	global_store_dwordx4 v[126:127], v[160:163], off offset:2048 sc1
	s_waitcnt lgkmcnt(0)
	global_store_dwordx4 v[126:127], v[164:167], off offset:3072 sc1
	v_rcp_f32_e32 v34, v132
	s_nop 1
	v_cmp_lt_f32_e32 vcc, 0, v132
	v_cndmask_b32_e32 v43, 0, v34, vcc
	s_waitcnt lgkmcnt(0)
	v_accvgpr_read_b32 v64, a16
	v_accvgpr_read_b32 v65, a17
	v_accvgpr_read_b32 v66, a18
	v_accvgpr_read_b32 v67, a19
	v_accvgpr_read_b32 v68, a20
	v_accvgpr_read_b32 v69, a21
	v_accvgpr_read_b32 v70, a22
	v_accvgpr_read_b32 v71, a23
	v_accvgpr_read_b32 v72, a24
	v_accvgpr_read_b32 v73, a25
	v_accvgpr_read_b32 v74, a26
	v_accvgpr_read_b32 v75, a27
	v_accvgpr_read_b32 v76, a28
	v_accvgpr_read_b32 v77, a29
	v_accvgpr_read_b32 v78, a30
	v_accvgpr_read_b32 v79, a31
	v_mul_f32_e32 v64, v64, v43
	v_mul_f32_e32 v65, v65, v43
	v_mul_f32_e32 v66, v66, v43
	v_mul_f32_e32 v67, v67, v43
	v_mul_f32_e32 v68, v68, v43
	v_mul_f32_e32 v69, v69, v43
	v_mul_f32_e32 v70, v70, v43
	v_mul_f32_e32 v71, v71, v43
	v_mul_f32_e32 v72, v72, v43
	v_mul_f32_e32 v73, v73, v43
	v_mul_f32_e32 v74, v74, v43
	v_mul_f32_e32 v75, v75, v43
	v_mul_f32_e32 v76, v76, v43
	v_mul_f32_e32 v77, v77, v43
	v_mul_f32_e32 v78, v78, v43
	v_mul_f32_e32 v79, v79, v43
	v_cvt_pk_f16_f32 v80, v64, v65
	v_cvt_pk_f16_f32 v81, v66, v67
	v_cvt_pk_f16_f32 v82, v68, v69
	v_cvt_pk_f16_f32 v83, v70, v71
	v_cvt_pk_f16_f32 v84, v72, v73
	v_cvt_pk_f16_f32 v85, v74, v75
	v_cvt_pk_f16_f32 v86, v76, v77
	v_cvt_pk_f16_f32 v87, v78, v79
	ds_write_b64 v100, v[80:81]
	ds_write_b64 v101, v[82:83]
	ds_write_b64 v102, v[84:85]
	ds_write_b64 v103, v[86:87]
	v_accvgpr_read_b32 v64, a48
	v_accvgpr_read_b32 v65, a49
	v_accvgpr_read_b32 v66, a50
	v_accvgpr_read_b32 v67, a51
	v_accvgpr_read_b32 v68, a52
	v_accvgpr_read_b32 v69, a53
	v_accvgpr_read_b32 v70, a54
	v_accvgpr_read_b32 v71, a55
	v_accvgpr_read_b32 v72, a56
	v_accvgpr_read_b32 v73, a57
	v_accvgpr_read_b32 v74, a58
	v_accvgpr_read_b32 v75, a59
	v_accvgpr_read_b32 v76, a60
	v_accvgpr_read_b32 v77, a61
	v_accvgpr_read_b32 v78, a62
	v_accvgpr_read_b32 v79, a63
	v_mul_f32_e32 v64, v64, v43
	v_mul_f32_e32 v65, v65, v43
	v_mul_f32_e32 v66, v66, v43
	v_mul_f32_e32 v67, v67, v43
	v_mul_f32_e32 v68, v68, v43
	v_mul_f32_e32 v69, v69, v43
	v_mul_f32_e32 v70, v70, v43
	v_mul_f32_e32 v71, v71, v43
	v_mul_f32_e32 v72, v72, v43
	v_mul_f32_e32 v73, v73, v43
	v_mul_f32_e32 v74, v74, v43
	v_mul_f32_e32 v75, v75, v43
	v_mul_f32_e32 v76, v76, v43
	v_mul_f32_e32 v77, v77, v43
	v_mul_f32_e32 v78, v78, v43
	v_mul_f32_e32 v79, v79, v43
	v_cvt_pk_f16_f32 v80, v64, v65
	v_cvt_pk_f16_f32 v81, v66, v67
	v_cvt_pk_f16_f32 v82, v68, v69
	v_cvt_pk_f16_f32 v83, v70, v71
	v_cvt_pk_f16_f32 v84, v72, v73
	v_cvt_pk_f16_f32 v85, v74, v75
	v_cvt_pk_f16_f32 v86, v76, v77
	v_cvt_pk_f16_f32 v87, v78, v79
	ds_write_b64 v104, v[80:81]
	ds_write_b64 v105, v[82:83]
	ds_write_b64 v106, v[84:85]
	ds_write_b64 v107, v[86:87]
	v_accvgpr_read_b32 v64, a80
	v_accvgpr_read_b32 v65, a81
	v_accvgpr_read_b32 v66, a82
	v_accvgpr_read_b32 v67, a83
	v_accvgpr_read_b32 v68, a84
	v_accvgpr_read_b32 v69, a85
	v_accvgpr_read_b32 v70, a86
	v_accvgpr_read_b32 v71, a87
	v_accvgpr_read_b32 v72, a88
	v_accvgpr_read_b32 v73, a89
	v_accvgpr_read_b32 v74, a90
	v_accvgpr_read_b32 v75, a91
	v_accvgpr_read_b32 v76, a92
	v_accvgpr_read_b32 v77, a93
	v_accvgpr_read_b32 v78, a94
	v_accvgpr_read_b32 v79, a95
	v_mul_f32_e32 v64, v64, v43
	v_mul_f32_e32 v65, v65, v43
	v_mul_f32_e32 v66, v66, v43
	v_mul_f32_e32 v67, v67, v43
	v_mul_f32_e32 v68, v68, v43
	v_mul_f32_e32 v69, v69, v43
	v_mul_f32_e32 v70, v70, v43
	v_mul_f32_e32 v71, v71, v43
	v_mul_f32_e32 v72, v72, v43
	v_mul_f32_e32 v73, v73, v43
	v_mul_f32_e32 v74, v74, v43
	v_mul_f32_e32 v75, v75, v43
	v_mul_f32_e32 v76, v76, v43
	v_mul_f32_e32 v77, v77, v43
	v_mul_f32_e32 v78, v78, v43
	v_mul_f32_e32 v79, v79, v43
	v_cvt_pk_f16_f32 v80, v64, v65
	v_cvt_pk_f16_f32 v81, v66, v67
	v_cvt_pk_f16_f32 v82, v68, v69
	v_cvt_pk_f16_f32 v83, v70, v71
	v_cvt_pk_f16_f32 v84, v72, v73
	v_cvt_pk_f16_f32 v85, v74, v75
	v_cvt_pk_f16_f32 v86, v76, v77
	v_cvt_pk_f16_f32 v87, v78, v79
	ds_write_b64 v108, v[80:81]
	ds_write_b64 v109, v[82:83]
	ds_write_b64 v110, v[84:85]
	ds_write_b64 v111, v[86:87]
	v_accvgpr_read_b32 v64, a112
	v_accvgpr_read_b32 v65, a113
	v_accvgpr_read_b32 v66, a114
	v_accvgpr_read_b32 v67, a115
	v_accvgpr_read_b32 v68, a116
	v_accvgpr_read_b32 v69, a117
	v_accvgpr_read_b32 v70, a118
	v_accvgpr_read_b32 v71, a119
	v_accvgpr_read_b32 v72, a120
	v_accvgpr_read_b32 v73, a121
	v_accvgpr_read_b32 v74, a122
	v_accvgpr_read_b32 v75, a123
	v_accvgpr_read_b32 v76, a124
	v_accvgpr_read_b32 v77, a125
	v_accvgpr_read_b32 v78, a126
	v_accvgpr_read_b32 v79, a127
	v_mul_f32_e32 v64, v64, v43
	v_mul_f32_e32 v65, v65, v43
	v_mul_f32_e32 v66, v66, v43
	v_mul_f32_e32 v67, v67, v43
	v_mul_f32_e32 v68, v68, v43
	v_mul_f32_e32 v69, v69, v43
	v_mul_f32_e32 v70, v70, v43
	v_mul_f32_e32 v71, v71, v43
	v_mul_f32_e32 v72, v72, v43
	v_mul_f32_e32 v73, v73, v43
	v_mul_f32_e32 v74, v74, v43
	v_mul_f32_e32 v75, v75, v43
	v_mul_f32_e32 v76, v76, v43
	v_mul_f32_e32 v77, v77, v43
	v_mul_f32_e32 v78, v78, v43
	v_mul_f32_e32 v79, v79, v43
	v_cvt_pk_f16_f32 v80, v64, v65
	v_cvt_pk_f16_f32 v81, v66, v67
	v_cvt_pk_f16_f32 v82, v68, v69
	v_cvt_pk_f16_f32 v83, v70, v71
	v_cvt_pk_f16_f32 v84, v72, v73
	v_cvt_pk_f16_f32 v85, v74, v75
	v_cvt_pk_f16_f32 v86, v76, v77
	v_cvt_pk_f16_f32 v87, v78, v79
	ds_write_b64 v112, v[80:81]
	ds_write_b64 v113, v[82:83]
	ds_write_b64 v114, v[84:85]
	ds_write_b64 v115, v[86:87]
	s_waitcnt lgkmcnt(0)
	ds_read_b128 v[136:139], v116
	ds_read_b128 v[140:143], v117
	ds_read_b128 v[144:147], v118
	ds_read_b128 v[148:151], v119
	ds_read_b128 v[152:155], v120
	ds_read_b128 v[156:159], v121
	ds_read_b128 v[160:163], v122
	ds_read_b128 v[164:167], v123
	s_waitcnt lgkmcnt(7)
	global_store_dwordx4 v[128:129], v[136:139], off sc1
	s_waitcnt lgkmcnt(6)
	global_store_dwordx4 v[128:129], v[140:143], off offset:1024 sc1
	s_waitcnt lgkmcnt(5)
	global_store_dwordx4 v[128:129], v[144:147], off offset:2048 sc1
	s_waitcnt lgkmcnt(4)
	global_store_dwordx4 v[128:129], v[148:151], off offset:3072 sc1
	s_waitcnt lgkmcnt(3)
	global_store_dwordx4 v[130:131], v[152:155], off sc1
	s_waitcnt lgkmcnt(2)
	global_store_dwordx4 v[130:131], v[156:159], off offset:1024 sc1
	s_waitcnt lgkmcnt(1)
	global_store_dwordx4 v[130:131], v[160:163], off offset:2048 sc1
	s_waitcnt lgkmcnt(0)
	global_store_dwordx4 v[130:131], v[164:167], off offset:3072 sc1
	s_waitcnt lgkmcnt(0)
	s_add_u32 s26, s26, s34
	s_addc_u32 s27, s27, 0
	v_cmp_gt_u64_e32 vcc, s[26:27], v[202:203]
	s_cbranch_vccnz .LBB2_64
	s_branch .LBB2_3
